# GDN prep item start: a_log/dt_bias loads issued with alpha/beta loads (one round trip instead of two)
# baseline (speedup 1.0000x reference)
; __device__ __forceinline__ float bf2f(bf16_t v) { return __uint_as_float(((unsigned)v) << 16); }
; __device__ __forceinline__ float fexp(float x) { return __builtin_amdgcn_exp2f(x * 1.4426950408889634f); }
; __device__ __forceinline__ float sigmoidf_(float x) { return __builtin_amdgcn_rcpf(1.f + fexp(-x)); }
; __device__ __forceinline__ float softplusf_(float x) { return x > 20.f ? x : 0.6931471805599453f * __builtin_amdgcn_logf(1.f + fexp(x)); }
; __device__ void phase_gdn_prep(const Params& p, int l, char* smem, int vb, int nvb, int pend, int oz) {
;     ...
;         if (tid < 128) {
;             const int dd = tid >> 6, t = tid & 63;
;             const size_t row = rowbase + t0 + t;
;             const float alpha = bf2f(U[row * LDU + C_GA + dd * 4 + h]);
;             const float beta = bf2f(U[row * LDU + C_GB + dd * 4 + h]);
;             gl[tid] = -1.4426950408889634f * fexp(p.in[I_GALOG][(l * 2 + dd) * 4 + h]) * softplusf_(alpha + p.in[I_GDT][(l * 2 + dd) * 4 + h]);
;             bl[tid] = sigmoidf_(beta);
;         }
.LBB0_521:
	s_or_b64 exec, exec, s[0:1]
	v_and_b32_e32 v60, 63, v8
	v_cmp_gt_u32_e32 vcc, s59, v9
	s_and_saveexec_b64 s[0:1], vcc
	s_cbranch_execz .LBB0_523
	s_ashr_i32 s25, s25, 5
	s_add_i32 s26, s25, s26
	s_ashr_i32 s27, s26, 31
	s_lshl_b64 s[38:39], s[26:27], 8
	s_add_u32 s25, s38, 0x4000
	s_addc_u32 s31, s39, 0
	s_lshl_b64 s[26:27], s[26:27], 11
	s_and_b64 s[28:29], s[28:29], exec
	s_cselect_b32 s27, s31, s27
	s_cselect_b32 s26, s25, s26
	s_ashr_i32 s25, s24, 31
	v_or_b32_e32 v4, s24, v60
	v_mov_b32_e32 v5, s25
	v_lshl_add_u64 v[4:5], v[4:5], 0, s[26:27]
	v_mov_b64_e32 v[6:7], s[34:35]
	v_mad_u64_u32 v[6:7], s[24:25], v4, s92, v[6:7]
	v_mad_i32_i24 v7, v5, s92, v7
	v_lshlrev_b32_e32 v2, 3, v11
	s_lshl_b32 s96, s3, 1
	v_lshl_add_u64 v[4:5], v[6:7], 0, v[2:3]
	v_lshl_add_u64 v[4:5], v[4:5], 0, s[96:97]
	v_add_co_u32_e32 v4, vcc, s22, v4
	s_or_b32 s3, s3, s8
	s_nop 0
	v_addc_co_u32_e32 v5, vcc, 0, v5, vcc
	global_load_ushort v2, v[4:5], off offset:2560
	global_load_ushort v12, v[4:5], off offset:2576
	v_readlane_b32 s40, v253, 18
	v_readlane_b32 s44, v253, 22
	v_readlane_b32 s45, v253, 23
	v_readlane_b32 s46, v253, 24
	v_readlane_b32 s47, v253, 25
	v_readlane_b32 s41, v253, 19
	v_readlane_b32 s42, v253, 20
	v_readlane_b32 s43, v253, 21
	v_readlane_b32 s48, v253, 26
	v_readlane_b32 s49, v253, 27
	v_readlane_b32 s50, v253, 28
	v_readlane_b32 s51, v253, 29
	v_readlane_b32 s52, v253, 30
	v_readlane_b32 s53, v253, 31
	v_readlane_b32 s54, v253, 32
	v_readlane_b32 s55, v253, 33
	v_lshl_or_b32 v4, v11, 2, s3
	v_ashrrev_i32_e32 v5, 31, v4
	v_lshlrev_b64 v[4:5], 2, v[4:5]
	v_lshl_add_u64 v[6:7], s[44:45], 0, v[4:5]
	v_lshl_add_u64 v[4:5], s[46:47], 0, v[4:5]
	global_load_dword v4, v[4:5], off
	s_mov_b32 s3, 0x41a00000
	global_load_dword v6, v[6:7], off
	s_waitcnt vmcnt(3)
	v_lshlrev_b32_e32 v2, 16, v2
	s_waitcnt vmcnt(2)
	v_lshlrev_b32_e32 v12, 16, v12
	s_waitcnt vmcnt(1)
	v_add_f32_e32 v2, v4, v2
	v_mul_f32_e32 v4, 0x3fb8aa3b, v2
	v_exp_f32_e32 v4, v4
	v_cmp_lt_f32_e32 vcc, s3, v2
	s_waitcnt vmcnt(0)
	v_mul_f32_e32 v6, 0x3fb8aa3b, v6
	v_exp_f32_e32 v6, v6
	v_add_f32_e32 v4, 1.0, v4
	v_log_f32_e32 v4, v4
	v_mul_f32_e32 v6, 0xbfb8aa3b, v6
	v_mul_f32_e32 v4, 0x3f317218, v4
	v_cndmask_b32_e32 v2, v4, v2, vcc
	v_mul_f32_e32 v4, 0xbfb8aa3b, v12
	v_exp_f32_e32 v4, v4
	v_mul_f32_e32 v2, v6, v2
	v_add_f32_e32 v4, 1.0, v4
	v_rcp_f32_e32 v4, v4
	ds_write2st64_b32 v10, v2, v4 offset0:220 offset1:222
